# attention item prologue: query-norm butterfly via DPP/permlane, key-norm table load issued before the query loads (on top of v72)
# baseline (speedup 1.0000x reference)
.LBB0_500:
	s_andn2_b64 vcc, exec, s[8:9]
	s_cbranch_vccnz .LBB0_411
	s_cmpk_gt_i32 s54, 0x3ff
	s_mov_b64 s[6:7], 0
	s_cbranch_scc1 .LBB0_410
	s_ashr_i32 s0, s54, 31
	s_lshr_b32 s1, s0, 28
	s_add_i32 s1, s54, s1
	s_ashr_i32 s6, s1, 4
	s_and_b32 s1, s1, 0x1fffff0
	s_sub_i32 s8, s54, s1
	s_lshr_b32 s1, s6, 29
	s_add_i32 s1, s6, s1
	s_and_b32 s1, s1, -8
	s_sub_i32 s10, s6, s1
	s_lshr_b32 s0, s0, 25
	s_add_i32 s54, s54, s0
	s_add_i32 s0, s10, 1
	v_cvt_f32_i32_e32 v2, s0
	s_mov_b32 s0, 0x42fc0000
	s_ashr_i32 s6, s54, 7
	v_mov_b32_e32 v82, v0
	v_cmp_lt_f32_e32 vcc, s0, v2
	s_and_b64 s[0:1], vcc, exec
	s_cselect_b32 s0, 0xffffffc0, 0
	v_cndmask_b32_e32 v4, 0, v214, vcc
	v_sub_f32_e32 v2, v4, v2
	v_exp_f32_e32 v2, v2
	s_ashr_i32 s7, s6, 31
	s_lshl_b32 s35, s8, 7
	s_mov_b32 s37, s55
	v_ldexp_f32 v4, v2, s0
	s_lshl_b64 s[0:1], s[6:7], 11
	s_ashr_i32 s7, s35, 31
	s_add_u32 s86, s0, s35
	s_addc_u32 s87, s1, s7
	s_mul_i32 s0, s87, 0x2c00
	s_mul_hi_u32 s1, s86, 0x2c00
	s_add_i32 s1, s1, s0
	s_mul_i32 s0, s86, 0x2c00
	s_add_u32 s7, s24, s0
	s_addc_u32 s8, s25, s1
	s_lshl_b32 s0, s10, 7
	s_ashr_i32 s1, s0, 31
	s_lshl_b64 s[88:89], s[0:1], 1
	s_add_u32 s0, s7, s88
	s_addc_u32 s1, s8, s89
	s_add_u32 s8, s0, 0x1400
	s_addc_u32 s9, s1, 0
	v_readfirstlane_b32 s55, v82
	s_ashr_i32 s82, s55, 7
	s_ashr_i32 s54, s55, 6
	v_and_b32_e32 v216, 31, v82
	s_lshl_b32 s0, s82, 5
	s_and_b32 s1, s54, 1
	v_or_b32_e32 v2, s0, v216
	v_mov_b64_e32 v[6:7], s[8:9]
	s_movk_i32 s7, 0x2c00
	v_bfe_u32 v221, v82, 5, 1
	v_mad_i64_i32 v[6:7], s[8:9], v2, s7, v[6:7]
	s_lshl_b32 s40, s1, 7
	v_lshl_add_u64 v[6:7], v[6:7], 0, s[40:41]
	v_lshlrev_b32_e32 v2, 4, v221
	v_lshl_add_u64 v[6:7], v[6:7], 0, v[2:3]
	s_lshl_b32 s44, s6, 3
	s_add_i32 s44, s44, s10
	s_ashr_i32 s45, s44, 31
	s_lshl_b64 s[44:45], s[44:45], 8
	v_readlane_b32 s46, v255, 13
	v_readlane_b32 s47, v255, 14
	v_and_b32_e32 v241, 63, v82
	s_add_u32 s44, s46, s44
	s_addc_u32 s45, s47, s45
	v_lshlrev_b32_e32 v241, 2, v241
	global_load_dword v240, v241, s[44:45] sc1
	global_load_dwordx4 v[130:133], v[6:7], off
	global_load_dwordx4 v[134:137], v[6:7], off offset:32
	global_load_dwordx4 v[138:141], v[6:7], off offset:64
	global_load_dwordx4 v[142:145], v[6:7], off offset:96
	v_and_b32_e32 v223, 63, v82
	s_barrier
	s_waitcnt vmcnt(3)
	v_and_b32_e32 v5, 0xffff0000, v130
	v_lshlrev_b32_e32 v2, 16, v130
	v_mul_f32_e32 v6, v5, v5
	v_fmac_f32_e32 v6, v2, v2
	v_lshlrev_b32_e32 v2, 16, v131
	v_fmac_f32_e32 v6, v2, v2
	v_and_b32_e32 v2, 0xffff0000, v131
	v_fmac_f32_e32 v6, v2, v2
	v_lshlrev_b32_e32 v2, 16, v132
	v_fmac_f32_e32 v6, v2, v2
	v_and_b32_e32 v2, 0xffff0000, v132
	v_fmac_f32_e32 v6, v2, v2
	v_lshlrev_b32_e32 v2, 16, v133
	v_fmac_f32_e32 v6, v2, v2
	v_and_b32_e32 v2, 0xffff0000, v133
	v_fmac_f32_e32 v6, v2, v2
	s_waitcnt vmcnt(2)
	v_lshlrev_b32_e32 v2, 16, v134
	v_fmac_f32_e32 v6, v2, v2
	v_and_b32_e32 v2, 0xffff0000, v134
	v_fmac_f32_e32 v6, v2, v2
	v_lshlrev_b32_e32 v2, 16, v135
	v_fmac_f32_e32 v6, v2, v2
	v_and_b32_e32 v2, 0xffff0000, v135
	v_fmac_f32_e32 v6, v2, v2
	v_lshlrev_b32_e32 v2, 16, v136
	v_fmac_f32_e32 v6, v2, v2
	v_and_b32_e32 v2, 0xffff0000, v136
	v_fmac_f32_e32 v6, v2, v2
	v_lshlrev_b32_e32 v2, 16, v137
	v_fmac_f32_e32 v6, v2, v2
	v_and_b32_e32 v2, 0xffff0000, v137
	v_fmac_f32_e32 v6, v2, v2
	s_waitcnt vmcnt(1)
	v_lshlrev_b32_e32 v2, 16, v138
	v_fmac_f32_e32 v6, v2, v2
	v_and_b32_e32 v2, 0xffff0000, v138
	v_fmac_f32_e32 v6, v2, v2
	v_lshlrev_b32_e32 v2, 16, v139
	v_fmac_f32_e32 v6, v2, v2
	v_and_b32_e32 v2, 0xffff0000, v139
	v_fmac_f32_e32 v6, v2, v2
	v_lshlrev_b32_e32 v2, 16, v140
	v_fmac_f32_e32 v6, v2, v2
	v_and_b32_e32 v2, 0xffff0000, v140
	v_fmac_f32_e32 v6, v2, v2
	v_lshlrev_b32_e32 v2, 16, v141
	v_fmac_f32_e32 v6, v2, v2
	v_and_b32_e32 v2, 0xffff0000, v141
	v_fmac_f32_e32 v6, v2, v2
	s_waitcnt vmcnt(0)
	v_lshlrev_b32_e32 v2, 16, v142
	v_fmac_f32_e32 v6, v2, v2
	v_and_b32_e32 v2, 0xffff0000, v142
	v_fmac_f32_e32 v6, v2, v2
	v_lshlrev_b32_e32 v2, 16, v143
	v_fmac_f32_e32 v6, v2, v2
	v_and_b32_e32 v2, 0xffff0000, v143
	v_fmac_f32_e32 v6, v2, v2
	v_lshlrev_b32_e32 v2, 16, v144
	v_fmac_f32_e32 v6, v2, v2
	v_and_b32_e32 v2, 0xffff0000, v144
	v_fmac_f32_e32 v6, v2, v2
	v_lshlrev_b32_e32 v2, 16, v145
	v_fmac_f32_e32 v6, v2, v2
	v_and_b32_e32 v2, 0xffff0000, v145
	v_and_b32_e32 v5, 64, v212
	v_fmac_f32_e32 v6, v2, v2
	v_xor_b32_e32 v2, 32, v212
	v_add_u32_e32 v5, 64, v5
	v_cmp_lt_i32_e32 vcc, v2, v5
	s_nop 1
	v_cndmask_b32_e32 v2, v212, v2, vcc
	v_lshlrev_b32_e32 v2, 2, v2
	v_mov_b32_e32 v7, v6
	s_nop 1
	v_permlane32_swap_b32_e32 v7, v6
	s_waitcnt lgkmcnt(0)
	v_add_f32_e32 v6, v6, v7
	v_xor_b32_e32 v7, 16, v212
	v_cmp_lt_i32_e32 vcc, v7, v5
	s_nop 1
	v_cndmask_b32_e32 v7, v212, v7, vcc
	v_lshlrev_b32_e32 v217, 2, v7
	v_mov_b32_e32 v7, v6
	s_nop 1
	v_permlane16_swap_b32_e32 v7, v6
	s_waitcnt lgkmcnt(0)
	v_max_f32_e32 v7, v7, v7
	v_max_f32_e32 v6, v6, v7
	v_xor_b32_e32 v7, 8, v212
	v_cmp_lt_i32_e32 vcc, v7, v5
	s_nop 1
	v_cndmask_b32_e32 v7, v212, v7, vcc
	v_lshlrev_b32_e32 v218, 2, v7
	s_nop 1
	v_mov_b32_dpp v7, v6 row_ror:8 row_mask:0xf bank_mask:0xf
	s_waitcnt lgkmcnt(0)
	v_max_f32_e32 v7, v7, v7
	v_max_f32_e32 v6, v6, v7
	v_xor_b32_e32 v7, 4, v212
	v_cmp_lt_i32_e32 vcc, v7, v5
	s_nop 1
	v_cndmask_b32_e32 v7, v212, v7, vcc
	v_lshlrev_b32_e32 v219, 2, v7
	s_nop 1
	v_mov_b32_dpp v7, v6 row_shr:4 row_mask:0xf bank_mask:0xa
	v_mov_b32_dpp v7, v6 row_shl:4 row_mask:0xf bank_mask:0x5
	s_waitcnt lgkmcnt(0)
	v_max_f32_e32 v7, v7, v7
	v_max_f32_e32 v6, v6, v7
	v_xor_b32_e32 v7, 2, v212
	v_cmp_lt_i32_e32 vcc, v7, v5
	s_nop 1
	v_cndmask_b32_e32 v7, v212, v7, vcc
	v_lshlrev_b32_e32 v220, 2, v7
	s_nop 1
	v_mov_b32_dpp v7, v6 quad_perm:[2,3,0,1] row_mask:0xf bank_mask:0xf
	s_waitcnt lgkmcnt(0)
	v_max_f32_e32 v7, v7, v7
	v_max_f32_e32 v6, v6, v7
	v_xor_b32_e32 v7, 1, v212
	v_cmp_lt_i32_e32 vcc, v7, v5
	s_nop 1
	v_cndmask_b32_e32 v5, v212, v7, vcc
	v_lshlrev_b32_e32 v222, 2, v5
	s_nop 1
	v_mov_b32_dpp v5, v6 quad_perm:[1,0,3,2] row_mask:0xf bank_mask:0xf
	v_cmp_eq_u32_e32 vcc, 0, v223
	s_and_saveexec_b64 s[8:9], vcc
	s_cbranch_execz .LBB0_504
	s_lshl_b32 s7, s54, 2
	s_add_i32 s7, s7, 0
	s_waitcnt lgkmcnt(0)
	v_max_f32_e32 v5, v5, v5
	v_max_f32_e32 v6, v6, v6
	s_add_i32 s7, s7, 0x18c00
	v_max_f32_e32 v5, v6, v5
	v_mov_b32_e32 v6, s7
	ds_write_b32 v6, v5
.LBB0_504:
	s_mov_b64 s[66:67], s[64:65]
	s_or_b64 exec, exec, s[8:9]
	s_mul_i32 s45, s6, 0x1600000
	s_mul_hi_i32 s44, s6, 0x1600000
	s_add_u32 s7, s24, s45
	s_addc_u32 s8, s25, s44
	s_add_u32 s11, s7, s88
	s_addc_u32 s31, s8, s89
	s_lshl_b32 s6, s6, 3
	s_add_i32 s6, s6, s10
	s_ashr_i32 s7, s6, 31
	s_lshl_b64 s[6:7], s[6:7], 8
	v_readlane_b32 s8, v255, 13
	v_readlane_b32 s9, v255, 14
	s_add_u32 s8, s8, s6
	s_addc_u32 s9, s9, s7
	s_add_i32 s6, 0, 0x18c00
	v_mul_f32_e32 v202, 0xbfb8aa3b, v4
	v_mov_b32_e32 v4, s6
	s_waitcnt lgkmcnt(0)
	s_barrier
	ds_read_b128 v[4:7], v4
	v_readlane_b32 s6, v255, 19
	s_mov_b32 s10, 0xf800000
	v_xor_b32_e32 v19, 0x80000000, v202
	v_bfe_u32 v83, v82, 2, 2
	s_waitcnt lgkmcnt(0)
	v_max_f32_e32 v5, v5, v5
	v_max_f32_e32 v4, v4, v4
	v_max_f32_e32 v4, v4, v5
	v_max3_f32 v8, v4, v6, v7
	v_mov_b32_e32 v4, s6
	ds_read_b128 v[4:7], v4
	v_and_b32_e32 v86, 3, v82
	s_waitcnt lgkmcnt(0)
	v_max3_f32 v4, v8, v4, v5
	v_max3_f32 v4, v4, v6, v7
	v_cmp_gt_f32_e32 vcc, s10, v4
	v_mul_f32_e32 v5, 0x4f800000, v4
	s_nop 0
	v_cndmask_b32_e32 v4, v4, v5, vcc
	v_sqrt_f32_e32 v5, v4
	s_nop 0
	v_add_u32_e32 v6, -1, v5
	v_fma_f32 v7, -v6, v5, v4
	v_cmp_ge_f32_e64 s[6:7], 0, v7
	v_add_u32_e32 v7, 1, v5
	s_nop 0
	v_cndmask_b32_e64 v6, v5, v6, s[6:7]
	v_fma_f32 v5, -v7, v5, v4
	v_cmp_lt_f32_e64 s[6:7], 0, v5
	s_nop 1
	v_cndmask_b32_e64 v5, v6, v7, s[6:7]
	v_mul_f32_e32 v6, 0x37800000, v5
	v_cndmask_b32_e32 v5, v5, v6, vcc
	v_cmp_class_f32_e32 vcc, v4, v1
	s_nop 1
	v_cndmask_b32_e32 v4, v5, v4, vcc
	v_lshlrev_b32_e32 v5, 2, v223
	v_mul_f32_e32 v4, 0x3f8147ae, v4
	s_waitcnt vmcnt(0)
	v_mov_b32_e32 v5, v240
	ds_bpermute_b32 v2, v2, v5
	v_max_f32_e32 v5, v5, v5
	s_waitcnt lgkmcnt(0)
	v_max_f32_e32 v2, v2, v2
	v_max_f32_e32 v2, v5, v2
	v_lshlrev_b32_e32 v5, 6, v216
	v_or_b32_e32 v6, 63, v5
	v_subrev_u32_e32 v5, s35, v5
	v_sub_u32_e32 v6, s35, v6
	v_max_i32_e32 v5, 0x7f, v5
	v_cmp_lt_i32_e32 vcc, 0, v6
	v_add_u32_e32 v5, 0xffffff81, v5
	s_nop 0
	v_cndmask_b32_e32 v6, v5, v6, vcc
	v_cmp_gt_f32_e32 vcc, s10, v2
	v_mul_f32_e32 v5, 0x4f800000, v2
	v_cvt_f32_u32_e32 v200, v6
	v_cndmask_b32_e32 v2, v2, v5, vcc
	v_sqrt_f32_e32 v5, v2
	s_nop 0
	v_add_u32_e32 v7, -1, v5
	v_fma_f32 v8, -v7, v5, v2
	v_cmp_ge_f32_e64 s[6:7], 0, v8
	v_add_u32_e32 v8, 1, v5
	s_nop 0
	v_cndmask_b32_e64 v7, v5, v7, s[6:7]
	v_fma_f32 v5, -v8, v5, v2
	v_cmp_lt_f32_e64 s[6:7], 0, v5
	s_nop 1
	v_cndmask_b32_e64 v5, v7, v8, s[6:7]
	v_mul_f32_e32 v7, 0x37800000, v5
	v_cndmask_b32_e32 v5, v5, v7, vcc
	v_cmp_class_f32_e32 vcc, v2, v1
	s_nop 1
	v_cndmask_b32_e32 v2, v5, v2, vcc
	v_mul_f32_e32 v2, v4, v2
	v_mul_f32_e32 v5, 0x3f8147ae, v2
	v_mov_b32_e32 v4, v19
	v_pk_mul_f32 v[4:5], v[4:5], v[200:201]
	s_nop 0
	v_add_f32_e32 v2, 0x41f00000, v5
	v_cmp_lt_f32_e32 vcc, v4, v2
	s_ff1_i32_b32 s46, vcc_lo
	s_flbit_i32_b32 s83, vcc_lo
	s_add_i32 s83, s83, s46
	s_mul_i32 s47, s46, 0xb0000
	s_add_u32 s9, s11, s47
	s_addc_u32 s8, s31, 0
	s_add_u32 s6, s9, 0x1c00
	s_addc_u32 s7, s8, 0
	s_lshl_b32 s11, s54, 7
	s_ashr_i32 s11, s11, 4
	s_lshl_b32 s10, s54, 3
	v_lshrrev_b32_e32 v2, 4, v223
	s_and_b32 s31, s11, -16
	s_lshr_b32 s11, s11, 1
	v_or_b32_e32 v4, s10, v2
	v_lshrrev_b32_e32 v5, 1, v82
	s_and_b32 s38, s11, 4
	s_movk_i32 s11, 0x2c00
	v_bitop3_b32 v6, s10, v82, v2 bitop3:0x36
	s_add_i32 s10, s0, s35
	v_and_b32_e32 v84, 8, v5
	v_mul_lo_u32 v7, v4, s11
	v_bitop3_b32 v4, v4, v82, 4 bitop3:0x36
	s_ashr_i32 s10, s10, 6
	v_or3_b32 v5, v84, v83, s31
	v_lshlrev_b32_e32 v6, 4, v6
	v_lshlrev_b32_e32 v4, 4, v4
	s_sub_i32 s40, s10, s46
	v_or_b32_e32 v5, s38, v5
	v_and_b32_e32 v85, 0xf0, v6
	v_and_b32_e32 v87, 0xf0, v4
	s_add_u32 s10, s9, 0x2400
	v_mul_lo_u32 v5, v5, s11
	v_or_b32_e32 v16, v85, v7
	v_lshrrev_b32_e32 v6, 3, v82
	v_or_b32_e32 v4, v7, v87
	s_addc_u32 s11, s8, 0
	s_lshl_b32 s8, s54, 11
	v_and_or_b32 v6, v6, 4, v86
	v_add_u32_e32 v22, 0xb000, v4
	s_add_i32 s34, s8, 0
	v_ashrrev_i32_e32 v17, 31, v16
	v_lshl_or_b32 v20, v6, 4, v5
	s_add_i32 m0, s34, 0xc000
	v_lshl_add_u64 v[4:5], s[6:7], 0, v[16:17]
	v_ashrrev_i32_e32 v23, 31, v22
	global_load_lds_dwordx4 v[4:5], off
	v_lshl_add_u64 v[4:5], s[6:7], 0, v[22:23]
	s_add_i32 m0, s34, 0xc400
	v_ashrrev_i32_e32 v21, 31, v20
	global_load_lds_dwordx4 v[4:5], off
	v_lshl_add_u64 v[4:5], s[10:11], 0, v[20:21]
	s_mov_b32 m0, s34
	s_mov_b64 s[8:9], 0x80
	global_load_lds_dwordx4 v[4:5], off
	v_lshl_add_u64 v[4:5], v[4:5], 0, s[8:9]
	s_add_i32 m0, s34, 0x400
	s_cmp_lt_u32 s83, 31
	global_load_lds_dwordx4 v[4:5], off
	s_cselect_b64 s[92:93], -1, 0
	s_cmp_gt_u32 s83, 30
	s_cbranch_scc1 .LBB0_506
	s_add_u32 s8, s6, 0xb0000
	s_addc_u32 s9, s7, 0
	v_lshl_add_u64 v[4:5], s[8:9], 0, v[16:17]
	v_lshl_add_u64 v[6:7], s[8:9], 0, v[22:23]
	s_add_i32 m0, s34, 0x10000
	s_add_i32 s8, s34, 0x10400
	global_load_lds_dwordx4 v[4:5], off
	s_mov_b32 m0, s8
	s_nop 0
	global_load_lds_dwordx4 v[6:7], off
